# grid barrier last hop: the XCD leader publishes XGEN(x) = gen+1 with a plain store (line kept in that XCD L2; only same-XCC workgroups poll it with sc1 loads) instead of a device-scope atomic add that
# speedup vs baseline: 1.0049x; 1.0049x over previous
.LBB0_190:
	s_or_b64 exec, exec, s[6:7]
	v_cvt_f32_u32_e32 v4, v2
	s_waitcnt vmcnt(0)
	v_readfirstlane_b32 s4, v3
	v_sub_u32_e32 v3, 0, v2
	v_rcp_iflag_f32_e32 v4, v4
	v_add_u32_e32 v5, s4, v1
	v_mul_f32_e32 v4, 0x4f7ffffe, v4
	v_cvt_u32_f32_e32 v4, v4
	v_mul_lo_u32 v1, v3, v4
	v_mul_hi_u32 v1, v4, v1
	v_add_u32_e32 v1, v4, v1
	v_mul_hi_u32 v1, v5, v1
	v_mul_lo_u32 v3, v1, v2
	v_sub_u32_e32 v3, v5, v3
	v_add_u32_e32 v4, 1, v1
	v_cmp_ge_u32_e32 vcc, v3, v2
	s_nop 1
	v_cndmask_b32_e32 v1, v1, v4, vcc
	v_sub_u32_e32 v4, v3, v2
	v_cndmask_b32_e32 v3, v3, v4, vcc
	v_add_u32_e32 v4, 1, v1
	v_cmp_ge_u32_e32 vcc, v3, v2
	v_add_u32_e32 v3, 1, v5
	s_nop 0
	v_cndmask_b32_e32 v1, v1, v4, vcc
	v_mul_lo_u32 v4, v2, v1
	v_add_u32_e32 v2, v4, v2
	v_readfirstlane_b32 s99, v1
	v_cmp_ne_u32_e32 vcc, v3, v2
	s_and_saveexec_b64 s[4:5], vcc
	s_xor_b64 s[4:5], exec, s[4:5]
	s_cbranch_execz .LBB0_204
	s_waitcnt lgkmcnt(0)
	v_mov_b32_e32 v0, 0x2000
	global_load_dword v0, v0, s[2:3] offset:1024 sc1
	s_add_u32 s8, s2, 0x2400
	s_addc_u32 s9, s3, 0
	s_waitcnt vmcnt(0)
	v_cmp_eq_u32_e32 vcc, v0, v1
	s_and_saveexec_b64 s[6:7], vcc
	s_cbranch_execz .LBB0_203
	s_mov_b32 s16, 1
	s_mov_b64 s[10:11], 0
	v_mov_b32_e32 v0, 0
	s_branch .LBB0_194

.LBB0_221:
	s_or_b64 exec, exec, s[4:5]
	s_mov_b64 s[4:5], exec
	v_mbcnt_lo_u32_b32 v0, s4, 0
	v_mbcnt_hi_u32_b32 v0, s5, v0
	v_cmp_eq_u32_e32 vcc, 0, v0
	s_waitcnt vmcnt(0)
	s_and_saveexec_b64 s[6:7], vcc
	s_cbranch_execz .LBB0_223
	s_bcnt1_i32_b64 s4, s[4:5]
	v_mov_b32_e32 v0, 0x2000
	s_add_i32 s99, s99, 1
	v_mov_b32_e32 v1, s99
	global_store_dword v0, v1, s[2:3] offset:1024

.LBB0_266:
	s_or_b64 exec, exec, s[8:9]
	v_cvt_f32_u32_e32 v4, v2
	s_waitcnt vmcnt(0)
	v_readfirstlane_b32 s6, v3
	v_sub_u32_e32 v3, 0, v2
	v_rcp_iflag_f32_e32 v4, v4
	v_add_u32_e32 v5, s6, v1
	v_mul_f32_e32 v4, 0x4f7ffffe, v4
	v_cvt_u32_f32_e32 v4, v4
	v_mul_lo_u32 v1, v3, v4
	v_mul_hi_u32 v1, v4, v1
	v_add_u32_e32 v1, v4, v1
	v_mul_hi_u32 v1, v5, v1
	v_mul_lo_u32 v3, v1, v2
	v_sub_u32_e32 v3, v5, v3
	v_add_u32_e32 v4, 1, v1
	v_cmp_ge_u32_e32 vcc, v3, v2
	s_nop 1
	v_cndmask_b32_e32 v1, v1, v4, vcc
	v_sub_u32_e32 v4, v3, v2
	v_cndmask_b32_e32 v3, v3, v4, vcc
	v_add_u32_e32 v4, 1, v1
	v_cmp_ge_u32_e32 vcc, v3, v2
	v_add_u32_e32 v3, 1, v5
	s_nop 0
	v_cndmask_b32_e32 v1, v1, v4, vcc
	v_mul_lo_u32 v4, v2, v1
	v_add_u32_e32 v2, v4, v2
	v_readfirstlane_b32 s99, v1
	v_cmp_ne_u32_e32 vcc, v3, v2
	s_and_saveexec_b64 s[6:7], vcc
	s_xor_b64 s[6:7], exec, s[6:7]
	s_cbranch_execz .LBB0_280
	s_waitcnt lgkmcnt(0)
	v_mov_b32_e32 v0, 0x2000
	global_load_dword v0, v0, s[2:3] offset:1024 sc1
	s_add_u32 s10, s2, 0x2400
	s_addc_u32 s11, s3, 0
	s_waitcnt vmcnt(0)
	v_cmp_eq_u32_e32 vcc, v0, v1
	s_and_saveexec_b64 s[8:9], vcc
	s_cbranch_execz .LBB0_279
	s_mov_b32 s16, 1
	s_mov_b64 s[12:13], 0
	v_mov_b32_e32 v0, 0
	s_branch .LBB0_270

.LBB0_297:
	s_or_b64 exec, exec, s[6:7]
	s_mov_b64 s[6:7], exec
	v_mbcnt_lo_u32_b32 v0, s6, 0
	v_mbcnt_hi_u32_b32 v0, s7, v0
	v_cmp_eq_u32_e32 vcc, 0, v0
	s_waitcnt vmcnt(0)
	s_and_saveexec_b64 s[8:9], vcc
	s_cbranch_execz .LBB0_299
	s_bcnt1_i32_b64 s6, s[6:7]
	v_mov_b32_e32 v0, 0x2000
	s_add_i32 s99, s99, 1
	v_mov_b32_e32 v1, s99
	global_store_dword v0, v1, s[2:3] offset:1024

.LBB0_690:
	s_or_b64 exec, exec, s[6:7]
	v_cvt_f32_u32_e32 v4, v2
	s_waitcnt vmcnt(0)
	v_readfirstlane_b32 s4, v3
	v_sub_u32_e32 v3, 0, v2
	v_rcp_iflag_f32_e32 v4, v4
	v_add_u32_e32 v5, s4, v1
	v_mul_f32_e32 v4, 0x4f7ffffe, v4
	v_cvt_u32_f32_e32 v4, v4
	v_mul_lo_u32 v1, v3, v4
	v_mul_hi_u32 v1, v4, v1
	v_add_u32_e32 v1, v4, v1
	v_mul_hi_u32 v1, v5, v1
	v_mul_lo_u32 v3, v1, v2
	v_sub_u32_e32 v3, v5, v3
	v_add_u32_e32 v4, 1, v1
	v_cmp_ge_u32_e32 vcc, v3, v2
	s_nop 1
	v_cndmask_b32_e32 v1, v1, v4, vcc
	v_sub_u32_e32 v4, v3, v2
	v_cndmask_b32_e32 v3, v3, v4, vcc
	v_add_u32_e32 v4, 1, v1
	v_cmp_ge_u32_e32 vcc, v3, v2
	v_add_u32_e32 v3, 1, v5
	s_nop 0
	v_cndmask_b32_e32 v1, v1, v4, vcc
	v_mul_lo_u32 v4, v2, v1
	v_add_u32_e32 v2, v4, v2
	v_readfirstlane_b32 s99, v1
	v_cmp_ne_u32_e32 vcc, v3, v2
	s_and_saveexec_b64 s[4:5], vcc
	s_xor_b64 s[4:5], exec, s[4:5]
	s_cbranch_execz .LBB0_704
	s_waitcnt lgkmcnt(0)
	v_mov_b32_e32 v0, 0x2000
	global_load_dword v0, v0, s[2:3] offset:1024 sc1
	s_add_u32 s10, s2, 0x2400
	s_addc_u32 s11, s3, 0
	s_waitcnt vmcnt(0)
	v_cmp_eq_u32_e32 vcc, v0, v1
	s_and_saveexec_b64 s[6:7], vcc
	s_cbranch_execz .LBB0_703
	s_mov_b32 s18, 1
	s_mov_b64 s[12:13], 0
	v_mov_b32_e32 v0, 0
	s_branch .LBB0_694

.LBB0_760:
	s_or_b64 exec, exec, s[6:7]
	v_cvt_f32_u32_e32 v4, v2
	s_waitcnt vmcnt(0)
	v_readfirstlane_b32 s4, v3
	v_sub_u32_e32 v3, 0, v2
	v_rcp_iflag_f32_e32 v4, v4
	v_add_u32_e32 v5, s4, v1
	v_mul_f32_e32 v4, 0x4f7ffffe, v4
	v_cvt_u32_f32_e32 v4, v4
	v_mul_lo_u32 v1, v3, v4
	v_mul_hi_u32 v1, v4, v1
	v_add_u32_e32 v1, v4, v1
	v_mul_hi_u32 v1, v5, v1
	v_mul_lo_u32 v3, v1, v2
	v_sub_u32_e32 v3, v5, v3
	v_add_u32_e32 v4, 1, v1
	v_cmp_ge_u32_e32 vcc, v3, v2
	s_nop 1
	v_cndmask_b32_e32 v1, v1, v4, vcc
	v_sub_u32_e32 v4, v3, v2
	v_cndmask_b32_e32 v3, v3, v4, vcc
	v_add_u32_e32 v4, 1, v1
	v_cmp_ge_u32_e32 vcc, v3, v2
	v_add_u32_e32 v3, 1, v5
	s_nop 0
	v_cndmask_b32_e32 v1, v1, v4, vcc
	v_mul_lo_u32 v4, v2, v1
	v_add_u32_e32 v2, v4, v2
	v_readfirstlane_b32 s99, v1
	v_cmp_ne_u32_e32 vcc, v3, v2
	s_and_saveexec_b64 s[4:5], vcc
	s_xor_b64 s[4:5], exec, s[4:5]
	s_cbranch_execz .LBB0_774
	s_waitcnt lgkmcnt(0)
	v_mov_b32_e32 v0, 0x2000
	global_load_dword v0, v0, s[2:3] offset:1024 sc1
	s_add_u32 s12, s2, 0x2400
	s_addc_u32 s13, s3, 0
	s_waitcnt vmcnt(0)
	v_cmp_eq_u32_e32 vcc, v0, v1
	s_and_saveexec_b64 s[6:7], vcc
	s_cbranch_execz .LBB0_773
	s_mov_b32 s18, 1
	s_mov_b64 s[14:15], 0
	v_mov_b32_e32 v0, 0
	s_branch .LBB0_764

.LBB0_858:
	s_or_b64 exec, exec, s[12:13]
	v_cvt_f32_u32_e32 v4, v2
	s_waitcnt vmcnt(0)
	v_readfirstlane_b32 s4, v3
	v_sub_u32_e32 v3, 0, v2
	v_rcp_iflag_f32_e32 v4, v4
	v_add_u32_e32 v5, s4, v1
	v_mul_f32_e32 v4, 0x4f7ffffe, v4
	v_cvt_u32_f32_e32 v4, v4
	v_mul_lo_u32 v1, v3, v4
	v_mul_hi_u32 v1, v4, v1
	v_add_u32_e32 v1, v4, v1
	v_mul_hi_u32 v1, v5, v1
	v_mul_lo_u32 v3, v1, v2
	v_sub_u32_e32 v3, v5, v3
	v_add_u32_e32 v4, 1, v1
	v_cmp_ge_u32_e32 vcc, v3, v2
	s_nop 1
	v_cndmask_b32_e32 v1, v1, v4, vcc
	v_sub_u32_e32 v4, v3, v2
	v_cndmask_b32_e32 v3, v3, v4, vcc
	v_add_u32_e32 v4, 1, v1
	v_cmp_ge_u32_e32 vcc, v3, v2
	v_add_u32_e32 v3, 1, v5
	s_nop 0
	v_cndmask_b32_e32 v1, v1, v4, vcc
	v_mul_lo_u32 v4, v2, v1
	v_add_u32_e32 v2, v4, v2
	v_readfirstlane_b32 s99, v1
	v_cmp_ne_u32_e32 vcc, v3, v2
	s_and_saveexec_b64 s[4:5], vcc
	s_xor_b64 s[4:5], exec, s[4:5]
	s_cbranch_execz .LBB0_872
	s_waitcnt lgkmcnt(0)
	v_mov_b32_e32 v0, 0x2000
	global_load_dword v0, v0, s[2:3] offset:1024 sc1
	s_add_u32 s14, s2, 0x2400
	s_addc_u32 s15, s3, 0
	s_waitcnt vmcnt(0)
	v_cmp_eq_u32_e32 vcc, v0, v1
	s_and_saveexec_b64 s[12:13], vcc
	s_cbranch_execz .LBB0_871
	s_mov_b32 s18, 1
	s_mov_b64 s[16:17], 0
	v_mov_b32_e32 v0, 0
	s_branch .LBB0_862

.LBB0_889:
	s_or_b64 exec, exec, s[4:5]
	s_mov_b64 s[4:5], exec
	v_mbcnt_lo_u32_b32 v0, s4, 0
	v_mbcnt_hi_u32_b32 v0, s5, v0
	v_cmp_eq_u32_e32 vcc, 0, v0
	s_waitcnt vmcnt(0)
	s_and_saveexec_b64 s[12:13], vcc
	s_cbranch_execz .LBB0_891
	s_bcnt1_i32_b64 s4, s[4:5]
	v_mov_b32_e32 v0, 0x2000
	s_add_i32 s99, s99, 1
	v_mov_b32_e32 v1, s99
	global_store_dword v0, v1, s[2:3] offset:1024

.LBB0_948:
	s_or_b64 exec, exec, s[12:13]
	v_cvt_f32_u32_e32 v4, v2
	s_waitcnt vmcnt(0)
	v_readfirstlane_b32 s6, v3
	v_sub_u32_e32 v3, 0, v2
	v_rcp_iflag_f32_e32 v4, v4
	v_add_u32_e32 v5, s6, v1
	v_mul_f32_e32 v4, 0x4f7ffffe, v4
	v_cvt_u32_f32_e32 v4, v4
	v_mul_lo_u32 v1, v3, v4
	v_mul_hi_u32 v1, v4, v1
	v_add_u32_e32 v1, v4, v1
	v_mul_hi_u32 v1, v5, v1
	v_mul_lo_u32 v3, v1, v2
	v_sub_u32_e32 v3, v5, v3
	v_add_u32_e32 v4, 1, v1
	v_cmp_ge_u32_e32 vcc, v3, v2
	s_nop 1
	v_cndmask_b32_e32 v1, v1, v4, vcc
	v_sub_u32_e32 v4, v3, v2
	v_cndmask_b32_e32 v3, v3, v4, vcc
	v_add_u32_e32 v4, 1, v1
	v_cmp_ge_u32_e32 vcc, v3, v2
	v_add_u32_e32 v3, 1, v5
	s_nop 0
	v_cndmask_b32_e32 v1, v1, v4, vcc
	v_mul_lo_u32 v4, v2, v1
	v_add_u32_e32 v2, v4, v2
	v_readfirstlane_b32 s99, v1
	v_cmp_ne_u32_e32 vcc, v3, v2
	s_and_saveexec_b64 s[6:7], vcc
	s_xor_b64 s[6:7], exec, s[6:7]
	s_cbranch_execz .LBB0_962
	s_waitcnt lgkmcnt(0)
	v_mov_b32_e32 v0, 0x2000
	global_load_dword v0, v0, s[4:5] offset:1024 sc1
	s_add_u32 s14, s4, 0x2400
	s_addc_u32 s15, s5, 0
	s_waitcnt vmcnt(0)
	v_cmp_eq_u32_e32 vcc, v0, v1
	s_and_saveexec_b64 s[12:13], vcc
	s_cbranch_execz .LBB0_961
	s_mov_b32 s18, 1
	s_mov_b64 s[16:17], 0
	v_mov_b32_e32 v0, 0
	s_branch .LBB0_952

.LBB0_979:
	s_or_b64 exec, exec, s[6:7]
	s_mov_b64 s[6:7], exec
	v_mbcnt_lo_u32_b32 v0, s6, 0
	v_mbcnt_hi_u32_b32 v0, s7, v0
	v_cmp_eq_u32_e32 vcc, 0, v0
	s_waitcnt vmcnt(0)
	s_and_saveexec_b64 s[12:13], vcc
	s_cbranch_execz .LBB0_981
	s_bcnt1_i32_b64 s6, s[6:7]
	v_mov_b32_e32 v0, 0x2000
	s_add_i32 s99, s99, 1
	v_mov_b32_e32 v1, s99
	global_store_dword v0, v1, s[4:5] offset:1024

.LBB0_1128:
	s_or_b64 exec, exec, s[6:7]
	v_cvt_f32_u32_e32 v4, v2
	s_waitcnt vmcnt(0)
	v_readfirstlane_b32 s4, v3
	v_sub_u32_e32 v3, 0, v2
	v_rcp_iflag_f32_e32 v4, v4
	v_add_u32_e32 v5, s4, v1
	v_mul_f32_e32 v4, 0x4f7ffffe, v4
	v_cvt_u32_f32_e32 v4, v4
	v_mul_lo_u32 v1, v3, v4
	v_mul_hi_u32 v1, v4, v1
	v_add_u32_e32 v1, v4, v1
	v_mul_hi_u32 v1, v5, v1
	v_mul_lo_u32 v3, v1, v2
	v_sub_u32_e32 v3, v5, v3
	v_add_u32_e32 v4, 1, v1
	v_cmp_ge_u32_e32 vcc, v3, v2
	s_nop 1
	v_cndmask_b32_e32 v1, v1, v4, vcc
	v_sub_u32_e32 v4, v3, v2
	v_cndmask_b32_e32 v3, v3, v4, vcc
	v_add_u32_e32 v4, 1, v1
	v_cmp_ge_u32_e32 vcc, v3, v2
	v_add_u32_e32 v3, 1, v5
	s_nop 0
	v_cndmask_b32_e32 v1, v1, v4, vcc
	v_mul_lo_u32 v4, v2, v1
	v_add_u32_e32 v2, v4, v2
	v_readfirstlane_b32 s99, v1
	v_cmp_ne_u32_e32 vcc, v3, v2
	s_and_saveexec_b64 s[4:5], vcc
	s_xor_b64 s[4:5], exec, s[4:5]
	s_cbranch_execz .LBB0_1142
	s_waitcnt lgkmcnt(0)
	v_mov_b32_e32 v0, 0x2000
	global_load_dword v0, v0, s[2:3] offset:1024 sc1
	s_add_u32 s8, s2, 0x2400
	s_addc_u32 s9, s3, 0
	s_waitcnt vmcnt(0)
	v_cmp_eq_u32_e32 vcc, v0, v1
	s_and_saveexec_b64 s[6:7], vcc
	s_cbranch_execz .LBB0_1141
	s_mov_b32 s18, 1
	s_mov_b64 s[10:11], 0
	v_mov_b32_e32 v0, 0
	s_branch .LBB0_1132

.LBB0_1735:
	s_or_b64 exec, exec, s[8:9]
	v_cvt_f32_u32_e32 v4, v2
	s_waitcnt vmcnt(0)
	v_readfirstlane_b32 s4, v3
	v_sub_u32_e32 v3, 0, v2
	v_rcp_iflag_f32_e32 v4, v4
	v_add_u32_e32 v5, s4, v1
	v_mul_f32_e32 v4, 0x4f7ffffe, v4
	v_cvt_u32_f32_e32 v4, v4
	v_mul_lo_u32 v1, v3, v4
	v_mul_hi_u32 v1, v4, v1
	v_add_u32_e32 v1, v4, v1
	v_mul_hi_u32 v1, v5, v1
	v_mul_lo_u32 v3, v1, v2
	v_sub_u32_e32 v3, v5, v3
	v_add_u32_e32 v4, 1, v1
	v_cmp_ge_u32_e32 vcc, v3, v2
	s_nop 1
	v_cndmask_b32_e32 v1, v1, v4, vcc
	v_sub_u32_e32 v4, v3, v2
	v_cndmask_b32_e32 v3, v3, v4, vcc
	v_add_u32_e32 v4, 1, v1
	v_cmp_ge_u32_e32 vcc, v3, v2
	v_add_u32_e32 v3, 1, v5
	s_nop 0
	v_cndmask_b32_e32 v1, v1, v4, vcc
	v_mul_lo_u32 v4, v2, v1
	v_add_u32_e32 v2, v4, v2
	v_readfirstlane_b32 s99, v1
	v_cmp_ne_u32_e32 vcc, v3, v2
	s_and_saveexec_b64 s[4:5], vcc
	s_xor_b64 s[4:5], exec, s[4:5]
	s_cbranch_execz .LBB0_1749
	s_waitcnt lgkmcnt(0)
	v_mov_b32_e32 v0, 0x2000
	global_load_dword v0, v0, s[2:3] offset:1024 sc1
	s_add_u32 s10, s2, 0x2400
	s_addc_u32 s11, s3, 0
	s_waitcnt vmcnt(0)
	v_cmp_eq_u32_e32 vcc, v0, v1
	s_and_saveexec_b64 s[8:9], vcc
	s_cbranch_execz .LBB0_1748
	s_mov_b32 s18, 1
	s_mov_b64 s[12:13], 0
	v_mov_b32_e32 v0, 0
	s_branch .LBB0_1739

.LBB0_1766:
	s_or_b64 exec, exec, s[4:5]
	s_mov_b64 s[4:5], exec
	v_mbcnt_lo_u32_b32 v0, s4, 0
	v_mbcnt_hi_u32_b32 v0, s5, v0
	v_cmp_eq_u32_e32 vcc, 0, v0
	s_waitcnt vmcnt(0)
	s_and_saveexec_b64 s[8:9], vcc
	s_cbranch_execz .LBB0_1768
	s_bcnt1_i32_b64 s4, s[4:5]
	v_mov_b32_e32 v0, 0x2000
	s_add_i32 s99, s99, 1
	v_mov_b32_e32 v1, s99
	global_store_dword v0, v1, s[2:3] offset:1024

.LBB0_1825:
	s_or_b64 exec, exec, s[8:9]
	v_cvt_f32_u32_e32 v4, v2
	s_waitcnt vmcnt(0)
	v_readfirstlane_b32 s6, v3
	v_sub_u32_e32 v3, 0, v2
	v_rcp_iflag_f32_e32 v4, v4
	v_add_u32_e32 v5, s6, v1
	v_mul_f32_e32 v4, 0x4f7ffffe, v4
	v_cvt_u32_f32_e32 v4, v4
	v_mul_lo_u32 v1, v3, v4
	v_mul_hi_u32 v1, v4, v1
	v_add_u32_e32 v1, v4, v1
	v_mul_hi_u32 v1, v5, v1
	v_mul_lo_u32 v3, v1, v2
	v_sub_u32_e32 v3, v5, v3
	v_add_u32_e32 v4, 1, v1
	v_cmp_ge_u32_e32 vcc, v3, v2
	s_nop 1
	v_cndmask_b32_e32 v1, v1, v4, vcc
	v_sub_u32_e32 v4, v3, v2
	v_cndmask_b32_e32 v3, v3, v4, vcc
	v_add_u32_e32 v4, 1, v1
	v_cmp_ge_u32_e32 vcc, v3, v2
	v_add_u32_e32 v3, 1, v5
	s_nop 0
	v_cndmask_b32_e32 v1, v1, v4, vcc
	v_mul_lo_u32 v4, v2, v1
	v_add_u32_e32 v2, v4, v2
	v_readfirstlane_b32 s99, v1
	v_cmp_ne_u32_e32 vcc, v3, v2
	s_and_saveexec_b64 s[6:7], vcc
	s_xor_b64 s[6:7], exec, s[6:7]
	s_cbranch_execz .LBB0_1839
	s_waitcnt lgkmcnt(0)
	v_mov_b32_e32 v0, 0x2000
	global_load_dword v0, v0, s[4:5] offset:1024 sc1
	s_add_u32 s10, s4, 0x2400
	s_addc_u32 s11, s5, 0
	s_waitcnt vmcnt(0)
	v_cmp_eq_u32_e32 vcc, v0, v1
	s_and_saveexec_b64 s[8:9], vcc
	s_cbranch_execz .LBB0_1838
	s_mov_b32 s18, 1
	s_mov_b64 s[12:13], 0
	v_mov_b32_e32 v0, 0
	s_branch .LBB0_1829

.LBB0_1856:
	s_or_b64 exec, exec, s[6:7]
	s_mov_b64 s[6:7], exec
	v_mbcnt_lo_u32_b32 v0, s6, 0
	v_mbcnt_hi_u32_b32 v0, s7, v0
	v_cmp_eq_u32_e32 vcc, 0, v0
	s_waitcnt vmcnt(0)
	s_and_saveexec_b64 s[8:9], vcc
	s_cbranch_execz .LBB0_1858
	s_bcnt1_i32_b64 s6, s[6:7]
	v_mov_b32_e32 v0, 0x2000
	s_add_i32 s99, s99, 1
	v_mov_b32_e32 v1, s99
	global_store_dword v0, v1, s[4:5] offset:1024

.LBB0_2327:
	s_or_b64 exec, exec, s[6:7]
	v_cvt_f32_u32_e32 v4, v2
	s_waitcnt vmcnt(0)
	v_readfirstlane_b32 s4, v3
	v_sub_u32_e32 v3, 0, v2
	v_rcp_iflag_f32_e32 v4, v4
	v_add_u32_e32 v5, s4, v1
	v_mul_f32_e32 v4, 0x4f7ffffe, v4
	v_cvt_u32_f32_e32 v4, v4
	v_mul_lo_u32 v1, v3, v4
	v_mul_hi_u32 v1, v4, v1
	v_add_u32_e32 v1, v4, v1
	v_mul_hi_u32 v1, v5, v1
	v_mul_lo_u32 v3, v1, v2
	v_sub_u32_e32 v3, v5, v3
	v_add_u32_e32 v4, 1, v1
	v_cmp_ge_u32_e32 vcc, v3, v2
	s_nop 1
	v_cndmask_b32_e32 v1, v1, v4, vcc
	v_sub_u32_e32 v4, v3, v2
	v_cndmask_b32_e32 v3, v3, v4, vcc
	v_add_u32_e32 v4, 1, v1
	v_cmp_ge_u32_e32 vcc, v3, v2
	v_add_u32_e32 v3, 1, v5
	s_nop 0
	v_cndmask_b32_e32 v1, v1, v4, vcc
	v_mul_lo_u32 v4, v2, v1
	v_add_u32_e32 v2, v4, v2
	v_readfirstlane_b32 s99, v1
	v_cmp_ne_u32_e32 vcc, v3, v2
	s_and_saveexec_b64 s[4:5], vcc
	s_xor_b64 s[4:5], exec, s[4:5]
	s_cbranch_execz .LBB0_2341
	s_waitcnt lgkmcnt(0)
	v_mov_b32_e32 v0, 0x2000
	global_load_dword v0, v0, s[2:3] offset:1024 sc1
	s_add_u32 s8, s2, 0x2400
	s_addc_u32 s9, s3, 0
	s_waitcnt vmcnt(0)
	v_cmp_eq_u32_e32 vcc, v0, v1
	s_and_saveexec_b64 s[6:7], vcc
	s_cbranch_execz .LBB0_2340
	s_mov_b32 s20, 1
	s_mov_b64 s[10:11], 0
	v_mov_b32_e32 v0, 0
	s_branch .LBB0_2331

.LBB0_2446:
	s_or_b64 exec, exec, s[6:7]
	v_cvt_f32_u32_e32 v4, v2
	s_waitcnt vmcnt(0)
	v_readfirstlane_b32 s4, v3
	v_sub_u32_e32 v3, 0, v2
	v_rcp_iflag_f32_e32 v4, v4
	v_add_u32_e32 v5, s4, v1
	v_mul_f32_e32 v4, 0x4f7ffffe, v4
	v_cvt_u32_f32_e32 v4, v4
	v_mul_lo_u32 v1, v3, v4
	v_mul_hi_u32 v1, v4, v1
	v_add_u32_e32 v1, v4, v1
	v_mul_hi_u32 v1, v5, v1
	v_mul_lo_u32 v3, v1, v2
	v_sub_u32_e32 v3, v5, v3
	v_add_u32_e32 v4, 1, v1
	v_cmp_ge_u32_e32 vcc, v3, v2
	s_nop 1
	v_cndmask_b32_e32 v1, v1, v4, vcc
	v_sub_u32_e32 v4, v3, v2
	v_cndmask_b32_e32 v3, v3, v4, vcc
	v_add_u32_e32 v4, 1, v1
	v_cmp_ge_u32_e32 vcc, v3, v2
	v_add_u32_e32 v3, 1, v5
	s_nop 0
	v_cndmask_b32_e32 v1, v1, v4, vcc
	v_mul_lo_u32 v4, v2, v1
	v_add_u32_e32 v2, v4, v2
	v_readfirstlane_b32 s99, v1
	v_cmp_ne_u32_e32 vcc, v3, v2
	s_and_saveexec_b64 s[4:5], vcc
	s_xor_b64 s[4:5], exec, s[4:5]
	s_cbranch_execz .LBB0_2460
	s_waitcnt lgkmcnt(0)
	v_mov_b32_e32 v0, 0x2000
	global_load_dword v0, v0, s[2:3] offset:1024 sc1
	s_add_u32 s8, s2, 0x2400
	s_addc_u32 s9, s3, 0
	s_waitcnt vmcnt(0)
	v_cmp_eq_u32_e32 vcc, v0, v1
	s_and_saveexec_b64 s[6:7], vcc
	s_cbranch_execz .LBB0_2459
	s_mov_b32 s24, 1
	s_mov_b64 s[10:11], 0
	v_mov_b32_e32 v0, 0
	s_branch .LBB0_2450

.LBB0_2516:
	s_or_b64 exec, exec, s[6:7]
	v_cvt_f32_u32_e32 v4, v2
	s_waitcnt vmcnt(0)
	v_readfirstlane_b32 s4, v3
	v_sub_u32_e32 v3, 0, v2
	v_rcp_iflag_f32_e32 v4, v4
	v_add_u32_e32 v5, s4, v1
	v_mul_f32_e32 v4, 0x4f7ffffe, v4
	v_cvt_u32_f32_e32 v4, v4
	v_mul_lo_u32 v1, v3, v4
	v_mul_hi_u32 v1, v4, v1
	v_add_u32_e32 v1, v4, v1
	v_mul_hi_u32 v1, v5, v1
	v_mul_lo_u32 v3, v1, v2
	v_sub_u32_e32 v3, v5, v3
	v_add_u32_e32 v4, 1, v1
	v_cmp_ge_u32_e32 vcc, v3, v2
	s_nop 1
	v_cndmask_b32_e32 v1, v1, v4, vcc
	v_sub_u32_e32 v4, v3, v2
	v_cndmask_b32_e32 v3, v3, v4, vcc
	v_add_u32_e32 v4, 1, v1
	v_cmp_ge_u32_e32 vcc, v3, v2
	v_add_u32_e32 v3, 1, v5
	s_nop 0
	v_cndmask_b32_e32 v1, v1, v4, vcc
	v_mul_lo_u32 v4, v2, v1
	v_add_u32_e32 v2, v4, v2
	v_readfirstlane_b32 s99, v1
	v_cmp_ne_u32_e32 vcc, v3, v2
	s_and_saveexec_b64 s[4:5], vcc
	s_xor_b64 s[4:5], exec, s[4:5]
	s_cbranch_execz .LBB0_2530
	s_waitcnt lgkmcnt(0)
	v_mov_b32_e32 v0, 0x2000
	global_load_dword v0, v0, s[2:3] offset:1024 sc1
	s_add_u32 s8, s2, 0x2400
	s_addc_u32 s9, s3, 0
	s_waitcnt vmcnt(0)
	v_cmp_eq_u32_e32 vcc, v0, v1
	s_and_saveexec_b64 s[6:7], vcc
	s_cbranch_execz .LBB0_2529
	s_mov_b32 s26, 1
	s_mov_b64 s[10:11], 0
	v_mov_b32_e32 v0, 0
	s_branch .LBB0_2520

.LBB0_2614:
	s_or_b64 exec, exec, s[8:9]
	v_cvt_f32_u32_e32 v4, v2
	s_waitcnt vmcnt(0)
	v_readfirstlane_b32 s4, v3
	v_sub_u32_e32 v3, 0, v2
	v_rcp_iflag_f32_e32 v4, v4
	v_add_u32_e32 v5, s4, v1
	v_mul_f32_e32 v4, 0x4f7ffffe, v4
	v_cvt_u32_f32_e32 v4, v4
	v_mul_lo_u32 v1, v3, v4
	v_mul_hi_u32 v1, v4, v1
	v_add_u32_e32 v1, v4, v1
	v_mul_hi_u32 v1, v5, v1
	v_mul_lo_u32 v3, v1, v2
	v_sub_u32_e32 v3, v5, v3
	v_add_u32_e32 v4, 1, v1
	v_cmp_ge_u32_e32 vcc, v3, v2
	s_nop 1
	v_cndmask_b32_e32 v1, v1, v4, vcc
	v_sub_u32_e32 v4, v3, v2
	v_cndmask_b32_e32 v3, v3, v4, vcc
	v_add_u32_e32 v4, 1, v1
	v_cmp_ge_u32_e32 vcc, v3, v2
	v_add_u32_e32 v3, 1, v5
	s_nop 0
	v_cndmask_b32_e32 v1, v1, v4, vcc
	v_mul_lo_u32 v4, v2, v1
	v_add_u32_e32 v2, v4, v2
	v_readfirstlane_b32 s99, v1
	v_cmp_ne_u32_e32 vcc, v3, v2
	s_and_saveexec_b64 s[4:5], vcc
	s_xor_b64 s[4:5], exec, s[4:5]
	s_cbranch_execz .LBB0_2628
	s_waitcnt lgkmcnt(0)
	v_mov_b32_e32 v0, 0x2000
	global_load_dword v0, v0, s[2:3] offset:1024 sc1
	s_add_u32 s10, s2, 0x2400
	s_addc_u32 s11, s3, 0
	s_waitcnt vmcnt(0)
	v_cmp_eq_u32_e32 vcc, v0, v1
	s_and_saveexec_b64 s[8:9], vcc
	s_cbranch_execz .LBB0_2627
	s_mov_b32 s28, 1
	s_mov_b64 s[12:13], 0
	v_mov_b32_e32 v0, 0
	s_branch .LBB0_2618

.LBB0_2704:
	s_or_b64 exec, exec, s[8:9]
	v_cvt_f32_u32_e32 v4, v2
	s_waitcnt vmcnt(0)
	v_readfirstlane_b32 s6, v3
	v_sub_u32_e32 v3, 0, v2
	v_rcp_iflag_f32_e32 v4, v4
	v_add_u32_e32 v5, s6, v1
	v_mul_f32_e32 v4, 0x4f7ffffe, v4
	v_cvt_u32_f32_e32 v4, v4
	v_mul_lo_u32 v1, v3, v4
	v_mul_hi_u32 v1, v4, v1
	v_add_u32_e32 v1, v4, v1
	v_mul_hi_u32 v1, v5, v1
	v_mul_lo_u32 v3, v1, v2
	v_sub_u32_e32 v3, v5, v3
	v_add_u32_e32 v4, 1, v1
	v_cmp_ge_u32_e32 vcc, v3, v2
	s_nop 1
	v_cndmask_b32_e32 v1, v1, v4, vcc
	v_sub_u32_e32 v4, v3, v2
	v_cndmask_b32_e32 v3, v3, v4, vcc
	v_add_u32_e32 v4, 1, v1
	v_cmp_ge_u32_e32 vcc, v3, v2
	v_add_u32_e32 v3, 1, v5
	s_nop 0
	v_cndmask_b32_e32 v1, v1, v4, vcc
	v_mul_lo_u32 v4, v2, v1
	v_add_u32_e32 v2, v4, v2
	v_readfirstlane_b32 s99, v1
	v_cmp_ne_u32_e32 vcc, v3, v2
	s_and_saveexec_b64 s[6:7], vcc
	s_xor_b64 s[6:7], exec, s[6:7]
	s_cbranch_execz .LBB0_2718
	s_waitcnt lgkmcnt(0)
	v_mov_b32_e32 v0, 0x2000
	global_load_dword v0, v0, s[4:5] offset:1024 sc1
	s_add_u32 s10, s4, 0x2400
	s_addc_u32 s11, s5, 0
	s_waitcnt vmcnt(0)
	v_cmp_eq_u32_e32 vcc, v0, v1
	s_and_saveexec_b64 s[8:9], vcc
	s_cbranch_execz .LBB0_2717
	s_mov_b32 s28, 1
	s_mov_b64 s[12:13], 0
	v_mov_b32_e32 v0, 0
	s_branch .LBB0_2708

.LBB0_2962:
	s_or_b64 exec, exec, s[8:9]
	v_cvt_f32_u32_e32 v4, v2
	s_waitcnt vmcnt(0)
	v_readfirstlane_b32 s6, v3
	v_sub_u32_e32 v3, 0, v2
	v_rcp_iflag_f32_e32 v4, v4
	v_add_u32_e32 v5, s6, v1
	v_mul_f32_e32 v4, 0x4f7ffffe, v4
	v_cvt_u32_f32_e32 v4, v4
	v_mul_lo_u32 v1, v3, v4
	v_mul_hi_u32 v1, v4, v1
	v_add_u32_e32 v1, v4, v1
	v_mul_hi_u32 v1, v5, v1
	v_mul_lo_u32 v3, v1, v2
	v_sub_u32_e32 v3, v5, v3
	v_add_u32_e32 v4, 1, v1
	v_cmp_ge_u32_e32 vcc, v3, v2
	s_nop 1
	v_cndmask_b32_e32 v1, v1, v4, vcc
	v_sub_u32_e32 v4, v3, v2
	v_cndmask_b32_e32 v3, v3, v4, vcc
	v_add_u32_e32 v4, 1, v1
	v_cmp_ge_u32_e32 vcc, v3, v2
	v_add_u32_e32 v3, 1, v5
	s_nop 0
	v_cndmask_b32_e32 v1, v1, v4, vcc
	v_mul_lo_u32 v4, v2, v1
	v_add_u32_e32 v2, v4, v2
	v_readfirstlane_b32 s99, v1
	v_cmp_ne_u32_e32 vcc, v3, v2
	s_and_saveexec_b64 s[6:7], vcc
	s_xor_b64 s[6:7], exec, s[6:7]
	s_cbranch_execz .LBB0_2976
	s_waitcnt lgkmcnt(0)
	v_mov_b32_e32 v0, 0x2000
	global_load_dword v0, v0, s[4:5] offset:1024 sc1
	s_add_u32 s10, s4, 0x2400
	s_addc_u32 s11, s5, 0
	s_waitcnt vmcnt(0)
	v_cmp_eq_u32_e32 vcc, v0, v1
	s_and_saveexec_b64 s[8:9], vcc
	s_cbranch_execz .LBB0_2975
	s_mov_b32 s22, 1
	s_mov_b64 s[12:13], 0
	v_mov_b32_e32 v0, 0
	s_branch .LBB0_2966

.LBB0_3194:
	s_or_b64 exec, exec, s[6:7]
	v_cvt_f32_u32_e32 v4, v2
	s_waitcnt vmcnt(0)
	v_readfirstlane_b32 s4, v3
	v_sub_u32_e32 v3, 0, v2
	v_rcp_iflag_f32_e32 v4, v4
	v_add_u32_e32 v5, s4, v1
	v_mul_f32_e32 v4, 0x4f7ffffe, v4
	v_cvt_u32_f32_e32 v4, v4
	v_mul_lo_u32 v1, v3, v4
	v_mul_hi_u32 v1, v4, v1
	v_add_u32_e32 v1, v4, v1
	v_mul_hi_u32 v1, v5, v1
	v_mul_lo_u32 v3, v1, v2
	v_sub_u32_e32 v3, v5, v3
	v_add_u32_e32 v4, 1, v1
	v_cmp_ge_u32_e32 vcc, v3, v2
	s_nop 1
	v_cndmask_b32_e32 v1, v1, v4, vcc
	v_sub_u32_e32 v4, v3, v2
	v_cndmask_b32_e32 v3, v3, v4, vcc
	v_add_u32_e32 v4, 1, v1
	v_cmp_ge_u32_e32 vcc, v3, v2
	v_add_u32_e32 v3, 1, v5
	s_nop 0
	v_cndmask_b32_e32 v1, v1, v4, vcc
	v_mul_lo_u32 v4, v2, v1
	v_add_u32_e32 v2, v4, v2
	v_readfirstlane_b32 s99, v1
	v_cmp_ne_u32_e32 vcc, v3, v2
	s_and_saveexec_b64 s[4:5], vcc
	s_xor_b64 s[4:5], exec, s[4:5]
	s_cbranch_execz .LBB0_3208
	s_waitcnt lgkmcnt(0)
	v_mov_b32_e32 v0, 0x2000
	global_load_dword v0, v0, s[2:3] offset:1024 sc1
	s_add_u32 s10, s2, 0x2400
	s_addc_u32 s11, s3, 0
	s_waitcnt vmcnt(0)
	v_cmp_eq_u32_e32 vcc, v0, v1
	s_and_saveexec_b64 s[6:7], vcc
	s_cbranch_execz .LBB0_3207
	s_mov_b32 s24, 1
	s_mov_b64 s[12:13], 0
	v_mov_b32_e32 v0, 0
	s_branch .LBB0_3198

.LBB0_3362:
	s_or_b64 exec, exec, s[8:9]
	v_cvt_f32_u32_e32 v4, v2
	s_waitcnt vmcnt(0)
	v_readfirstlane_b32 s4, v3
	v_sub_u32_e32 v3, 0, v2
	v_rcp_iflag_f32_e32 v4, v4
	v_add_u32_e32 v5, s4, v1
	v_mul_f32_e32 v4, 0x4f7ffffe, v4
	v_cvt_u32_f32_e32 v4, v4
	v_mul_lo_u32 v1, v3, v4
	v_mul_hi_u32 v1, v4, v1
	v_add_u32_e32 v1, v4, v1
	v_mul_hi_u32 v1, v5, v1
	v_mul_lo_u32 v3, v1, v2
	v_sub_u32_e32 v3, v5, v3
	v_add_u32_e32 v4, 1, v1
	v_cmp_ge_u32_e32 vcc, v3, v2
	s_nop 1
	v_cndmask_b32_e32 v1, v1, v4, vcc
	v_sub_u32_e32 v4, v3, v2
	v_cndmask_b32_e32 v3, v3, v4, vcc
	v_add_u32_e32 v4, 1, v1
	v_cmp_ge_u32_e32 vcc, v3, v2
	v_add_u32_e32 v3, 1, v5
	s_nop 0
	v_cndmask_b32_e32 v1, v1, v4, vcc
	v_mul_lo_u32 v4, v2, v1
	v_add_u32_e32 v2, v4, v2
	v_readfirstlane_b32 s99, v1
	v_cmp_ne_u32_e32 vcc, v3, v2
	s_and_saveexec_b64 s[4:5], vcc
	s_xor_b64 s[4:5], exec, s[4:5]
	s_cbranch_execz .LBB0_3376
	s_waitcnt lgkmcnt(0)
	v_mov_b32_e32 v0, 0x2000
	global_load_dword v0, v0, s[2:3] offset:1024 sc1
	s_add_u32 s10, s2, 0x2400
	s_addc_u32 s11, s3, 0
	s_waitcnt vmcnt(0)
	v_cmp_eq_u32_e32 vcc, v0, v1
	s_and_saveexec_b64 s[8:9], vcc
	s_cbranch_execz .LBB0_3375
	s_mov_b32 s26, 1
	s_mov_b64 s[12:13], 0
	v_mov_b32_e32 v0, 0
	s_branch .LBB0_3366

.LBB0_3452:
	s_or_b64 exec, exec, s[8:9]
	v_cvt_f32_u32_e32 v4, v2
	s_waitcnt vmcnt(0)
	v_readfirstlane_b32 s6, v3
	v_sub_u32_e32 v3, 0, v2
	v_rcp_iflag_f32_e32 v4, v4
	v_add_u32_e32 v5, s6, v1
	v_mul_f32_e32 v4, 0x4f7ffffe, v4
	v_cvt_u32_f32_e32 v4, v4
	v_mul_lo_u32 v1, v3, v4
	v_mul_hi_u32 v1, v4, v1
	v_add_u32_e32 v1, v4, v1
	v_mul_hi_u32 v1, v5, v1
	v_mul_lo_u32 v3, v1, v2
	v_sub_u32_e32 v3, v5, v3
	v_add_u32_e32 v4, 1, v1
	v_cmp_ge_u32_e32 vcc, v3, v2
	s_nop 1
	v_cndmask_b32_e32 v1, v1, v4, vcc
	v_sub_u32_e32 v4, v3, v2
	v_cndmask_b32_e32 v3, v3, v4, vcc
	v_add_u32_e32 v4, 1, v1
	v_cmp_ge_u32_e32 vcc, v3, v2
	v_add_u32_e32 v3, 1, v5
	s_nop 0
	v_cndmask_b32_e32 v1, v1, v4, vcc
	v_mul_lo_u32 v4, v2, v1
	v_add_u32_e32 v2, v4, v2
	v_readfirstlane_b32 s99, v1
	v_cmp_ne_u32_e32 vcc, v3, v2
	s_and_saveexec_b64 s[6:7], vcc
	s_xor_b64 s[6:7], exec, s[6:7]
	s_cbranch_execz .LBB0_3466
	s_waitcnt lgkmcnt(0)
	v_mov_b32_e32 v0, 0x2000
	global_load_dword v0, v0, s[4:5] offset:1024 sc1
	s_add_u32 s10, s4, 0x2400
	s_addc_u32 s11, s5, 0
	s_waitcnt vmcnt(0)
	v_cmp_eq_u32_e32 vcc, v0, v1
	s_and_saveexec_b64 s[8:9], vcc
	s_cbranch_execz .LBB0_3465
	s_mov_b32 s26, 1
	s_mov_b64 s[12:13], 0
	v_mov_b32_e32 v0, 0
	s_branch .LBB0_3456
